# nt cache policy on the MoE weight (B operand) LDS-DMA loads in GU/DN K-loops of both layers
# baseline (speedup 1.0000x reference)
; #define PG8_STAGE(bufoff, gbase, voff) do { _Pragma("unroll") for (int _i = 0; _i < 2; ++_i) \
;         __builtin_amdgcn_global_load_lds((const unsigned*)((const char*)(gbase) + (voff)[_i]), (LAS unsigned*)(lds + (bufoff) + ldsw + _i * 8192), 16, 0, 0); } while (0)
; #define PG8_LDA(dst, b, h) do { _Pragma("unroll") for (int m = 0; m < 4; ++m) _Pragma("unroll") for (int k = 0; k < 2; ++k) dst[m][k] = *(const LAS bf16x8*)(lds + PG8_SA(b, h) + ((aoff ^ (k * 64)) + m * 2048)); } while (0)
; #define PG8_LDB(dst, b, h) do { _Pragma("unroll") for (int n = 0; n < 2; ++n) _Pragma("unroll") for (int k = 0; k < 2; ++k) dst[n][k] = *(const LAS bf16x8*)(lds + PG8_SB(b, h) + ((boff ^ (k * 64)) + n * 2048)); } while (0)
; #define PG8_BAR __builtin_amdgcn_s_barrier()
;     ...
;             const bool last = (t == nt - 2);
;             const char* a1 = cA + (size_t)(t + 1) * kstepA;
;             const char* a2 = last ? nA : cA + (size_t)(t + 2) * kstepA; const char* b2 = last ? nB : cB + (size_t)(t + 2) * kstepB;
;             const char* a3 = a2 + kstepA; const char* b3 = b2 + kstepB;
;             unsigned vs[2][2];
;             if constexpr (GATHER) {
;                 if (last && has_next) {
; #pragma unroll
;                     for (int hh = 0; hh < 2; ++hh)
; #pragma unroll
;                         for (int i = 0; i < 2; ++i) voffN[hh][i] = (unsigned)idxl[(ui + 1) * 256 + hh * HALF + sR[i]] * (unsigned)(K * 2) + (unsigned)sC[i] * 2u;
;                 }
; #pragma unroll
;                 for (int hh = 0; hh < 2; ++hh)
; #pragma unroll
;                     for (int i = 0; i < 2; ++i) vs[hh][i] = last ? voffN[hh][i] : voffA[hh][i];
;             } else {
; #pragma unroll
;                 for (int hh = 0; hh < 2; ++hh)
; #pragma unroll
;                     for (int i = 0; i < 2; ++i) vs[hh][i] = voffA[hh][i];
;             }
;             PG8_LDB(B0, 0, 0); PG8_LDB(B1, 0, 1); PG8_SCHED; PG8_LDA(At, 0, 0); PG8_STAGE(PG8_SA(1, 1), a1, voffA[1]);
;             PG8_WAIT_V(8); PG8_WAIT_L(0); PG8_BAR; if (do0) { PG8_MMA(0, 0, At, B0); PG8_MMA(0, 1, At, B1); } PG8_BAR; PG8_SCHED;
;             PG8_LDA(At, 0, 1); PG8_STAGE(PG8_SB(0, 0), b2, voffB); PG8_STAGE(PG8_SB(0, 1), b2 + hstep, voffB); PG8_STAGE(PG8_SA(0, 0), a2, vs[0]);
;             PG8_WAIT_V(8); PG8_WAIT_L(0); PG8_BAR; if (do1) { PG8_MMA(1, 0, At, B0); PG8_MMA(1, 1, At, B1); } PG8_BAR; PG8_SCHED;
.LBB0_1010:
	s_add_u32 s10, s90, s28
	s_addc_u32 s11, s91, s29
	s_add_u32 s30, s10, 0x4213700
	s_addc_u32 s31, s11, 0
	s_and_b64 s[10:11], s[6:7], exec
	v_cndmask_b32_e64 v2, v218, v4, s[6:7]
	v_cndmask_b32_e64 v224, v219, v5, s[6:7]
	s_cselect_b32 s35, s83, s31
	s_cselect_b32 s34, s82, s30
	s_cselect_b32 s31, s21, s64
	s_cselect_b32 s30, s20, s19
	s_barrier
	s_mov_b32 m0, s37
	v_lshl_add_u64 v[232:233], s[30:31], 0, v[202:203]
	s_add_u32 s10, s30, 0x40000
	s_waitcnt lgkmcnt(0)
	ds_read_b128 v[190:193], v228 offset:16384
	ds_read_b128 v[178:181], v228 offset:18432
	ds_read_b128 v[194:197], v229 offset:16384
	ds_read_b128 v[182:185], v229 offset:18432
	ds_read_b128 v[174:177], v228 offset:20480
	ds_read_b128 v[166:169], v228 offset:22528
	ds_read_b128 v[186:189], v229 offset:20480
	ds_read_b128 v[170:173], v229 offset:22528
	global_load_lds_dwordx4 v[232:233], off nt
	v_lshl_add_u64 v[232:233], s[30:31], 0, v[204:205]
	s_mov_b32 m0, s38
	s_addc_u32 s11, s31, 0
	global_load_lds_dwordx4 v[232:233], off nt
	v_lshl_add_u64 v[232:233], s[10:11], 0, v[202:203]
	s_mov_b32 m0, s39
	v_cndmask_b32_e64 v213, 0, 1, s[24:25]
	global_load_lds_dwordx4 v[232:233], off nt
	v_lshl_add_u64 v[232:233], s[10:11], 0, v[204:205]
	s_mov_b32 m0, s40
	v_cmp_ne_u32_e64 s[10:11], 1, v213
	global_load_lds_dwordx4 v[232:233], off nt
	s_mov_b32 m0, s23
	s_andn2_b64 vcc, exec, s[24:25]
	global_load_lds_dwordx4 v2, s[34:35]
	s_mov_b32 m0, s41
	s_nop 0
	global_load_lds_dwordx4 v224, s[34:35]
	s_waitcnt vmcnt(8)
	s_waitcnt lgkmcnt(0)
	s_barrier
	s_cbranch_vccnz .LBB0_1012
	s_setprio 1
	s_waitcnt lgkmcnt(0)
	v_mfma_f32_16x16x32_bf16 v[66:69], v[150:153], v[190:193], v[66:69]
	v_mfma_f32_16x16x32_bf16 v[62:65], v[158:161], v[190:193], v[62:65]
	v_mfma_f32_16x16x32_bf16 v[50:53], v[150:153], v[178:181], v[50:53]
	v_mfma_f32_16x16x32_bf16 v[46:49], v[158:161], v[178:181], v[46:49]
	v_mfma_f32_16x16x32_bf16 v[34:37], v[150:153], v[174:177], v[34:37]
	v_mfma_f32_16x16x32_bf16 v[30:33], v[158:161], v[174:177], v[30:33]
	v_mfma_f32_16x16x32_bf16 v[18:21], v[150:153], v[166:169], v[18:21]
	v_mfma_f32_16x16x32_bf16 v[14:17], v[158:161], v[166:169], v[14:17]
	v_mfma_f32_16x16x32_bf16 v[66:69], v[154:157], v[194:197], v[66:69]
	v_mfma_f32_16x16x32_bf16 v[62:65], v[162:165], v[194:197], v[62:65]
	v_mfma_f32_16x16x32_bf16 v[50:53], v[154:157], v[182:185], v[50:53]
	v_mfma_f32_16x16x32_bf16 v[46:49], v[162:165], v[182:185], v[46:49]
	v_mfma_f32_16x16x32_bf16 v[34:37], v[154:157], v[186:189], v[34:37]
	v_mfma_f32_16x16x32_bf16 v[30:33], v[162:165], v[186:189], v[30:33]
	v_mfma_f32_16x16x32_bf16 v[18:21], v[154:157], v[170:173], v[18:21]
	v_mfma_f32_16x16x32_bf16 v[14:17], v[162:165], v[170:173], v[14:17]
	s_setprio 0
	s_setprio 1
	v_mfma_f32_16x16x32_bf16 v[58:61], v[134:137], v[190:193], v[58:61]
	v_mfma_f32_16x16x32_bf16 v[54:57], v[142:145], v[190:193], v[54:57]
	v_mfma_f32_16x16x32_bf16 v[42:45], v[134:137], v[178:181], v[42:45]
	v_mfma_f32_16x16x32_bf16 v[38:41], v[142:145], v[178:181], v[38:41]
	v_mfma_f32_16x16x32_bf16 v[26:29], v[134:137], v[174:177], v[26:29]
	v_mfma_f32_16x16x32_bf16 v[22:25], v[142:145], v[174:177], v[22:25]
	v_mfma_f32_16x16x32_bf16 v[10:13], v[134:137], v[166:169], v[10:13]
	v_mfma_f32_16x16x32_bf16 v[6:9], v[142:145], v[166:169], v[6:9]
	v_mfma_f32_16x16x32_bf16 v[58:61], v[138:141], v[194:197], v[58:61]
	v_mfma_f32_16x16x32_bf16 v[54:57], v[146:149], v[194:197], v[54:57]
	v_mfma_f32_16x16x32_bf16 v[42:45], v[138:141], v[182:185], v[42:45]
	v_mfma_f32_16x16x32_bf16 v[38:41], v[146:149], v[182:185], v[38:41]
	v_mfma_f32_16x16x32_bf16 v[26:29], v[138:141], v[186:189], v[26:29]
	v_mfma_f32_16x16x32_bf16 v[22:25], v[146:149], v[186:189], v[22:25]
	v_mfma_f32_16x16x32_bf16 v[10:13], v[138:141], v[170:173], v[10:13]
	v_mfma_f32_16x16x32_bf16 v[6:9], v[146:149], v[170:173], v[6:9]
	s_setprio 0

; #define PG8_STAGE(bufoff, gbase, voff) do { _Pragma("unroll") for (int _i = 0; _i < 2; ++_i) \
;         __builtin_amdgcn_global_load_lds((const unsigned*)((const char*)(gbase) + (voff)[_i]), (LAS unsigned*)(lds + (bufoff) + ldsw + _i * 8192), 16, 0, 0); } while (0)
; #define PG8_LDA(dst, b, h) do { _Pragma("unroll") for (int m = 0; m < 4; ++m) _Pragma("unroll") for (int k = 0; k < 2; ++k) dst[m][k] = *(const LAS bf16x8*)(lds + PG8_SA(b, h) + ((aoff ^ (k * 64)) + m * 2048)); } while (0)
;     ...
;             const char* a3 = a2 + kstepA; const char* b3 = b2 + kstepB;
;             unsigned vs[2][2];
;             if constexpr (GATHER) {
;                 if (last && has_next) {
; #pragma unroll
;                     for (int hh = 0; hh < 2; ++hh)
; #pragma unroll
;                         for (int i = 0; i < 2; ++i) voffN[hh][i] = (unsigned)idxl[(ui + 1) * 256 + hh * HALF + sR[i]] * (unsigned)(K * 2) + (unsigned)sC[i] * 2u;
;                 }
; #pragma unroll
;                 for (int hh = 0; hh < 2; ++hh)
; #pragma unroll
;                     for (int i = 0; i < 2; ++i) vs[hh][i] = last ? voffN[hh][i] : voffA[hh][i];
;             } else {
; #pragma unroll
;                 for (int hh = 0; hh < 2; ++hh)
; #pragma unroll
;                     for (int i = 0; i < 2; ++i) vs[hh][i] = voffA[hh][i];
;             }
;             PG8_LDB(B0, 0, 0); PG8_LDB(B1, 0, 1); PG8_SCHED; PG8_LDA(At, 0, 0); PG8_STAGE(PG8_SA(1, 1), a1, voffA[1]);
;             PG8_WAIT_V(8); PG8_WAIT_L(0); PG8_BAR; if (do0) { PG8_MMA(0, 0, At, B0); PG8_MMA(0, 1, At, B1); } PG8_BAR; PG8_SCHED;
;             PG8_LDA(At, 0, 1); PG8_STAGE(PG8_SB(0, 0), b2, voffB); PG8_STAGE(PG8_SB(0, 1), b2 + hstep, voffB); PG8_STAGE(PG8_SA(0, 0), a2, vs[0]);
;             PG8_WAIT_V(8); PG8_WAIT_L(0); PG8_BAR; if (do1) { PG8_MMA(1, 0, At, B0); PG8_MMA(1, 1, At, B1); } PG8_BAR; PG8_SCHED;
;             PG8_LDB(B0, 1, 0); PG8_LDB(B1, 1, 1); PG8_SCHED; PG8_LDA(At, 1, 0); PG8_STAGE(PG8_SA(0, 1), a2, vs[1]);
;             PG8_WAIT_V(8); PG8_WAIT_L(0); PG8_BAR; if (do0) { PG8_MMA(0, 0, At, B0); PG8_MMA(0, 1, At, B1); } PG8_BAR; PG8_SCHED;
;             PG8_LDA(At, 1, 1); PG8_STAGE(PG8_SB(1, 0), b3, voffB); PG8_STAGE(PG8_SB(1, 1), b3 + hstep, voffB); PG8_STAGE(PG8_SA(1, 0), a3, vs[0]);
;             PG8_WAIT_V(8); PG8_WAIT_L(0); PG8_BAR; if (do1) { PG8_MMA(1, 0, At, B0); PG8_MMA(1, 1, At, B1); } PG8_BAR; PG8_SCHED;
.LBB0_1014:
	v_mov_b32_e32 v225, v3
	s_add_u32 s6, s30, 0x4000
	v_lshl_add_u64 v[232:233], s[34:35], 0, v[2:3]
	v_lshl_add_u64 v[224:225], s[34:35], 0, v[224:225]
	s_addc_u32 s7, s31, 0
	s_barrier
	s_mov_b32 m0, s47
	v_lshl_add_u64 v[234:235], s[6:7], 0, v[202:203]
	s_waitcnt lgkmcnt(0)
	ds_read_b128 v[190:193], v228 offset:49152
	ds_read_b128 v[178:181], v228 offset:51200
	ds_read_b128 v[194:197], v229 offset:49152
	ds_read_b128 v[182:185], v229 offset:51200
	ds_read_b128 v[174:177], v228 offset:53248
	ds_read_b128 v[166:169], v228 offset:55296
	ds_read_b128 v[186:189], v229 offset:53248
	ds_read_b128 v[170:173], v229 offset:55296
	global_load_lds_dwordx4 v[234:235], off nt
	v_lshl_add_u64 v[234:235], s[6:7], 0, v[204:205]
	s_add_u32 s6, s30, 0x44000
	s_mov_b32 m0, s48
	s_addc_u32 s7, s31, 0
	global_load_lds_dwordx4 v[234:235], off nt
	v_lshl_add_u64 v[234:235], s[6:7], 0, v[202:203]
	s_mov_b32 m0, s51
	v_lshl_add_u64 v[232:233], v[232:233], 0, s[16:17]
	global_load_lds_dwordx4 v[234:235], off nt
	v_lshl_add_u64 v[234:235], s[6:7], 0, v[204:205]
	s_mov_b32 m0, s52
	v_lshl_add_u64 v[224:225], v[224:225], 0, s[16:17]
	global_load_lds_dwordx4 v[234:235], off nt
	s_mov_b32 m0, s49
	s_and_b64 vcc, exec, s[10:11]
	global_load_lds_dwordx4 v[232:233], off
	s_mov_b32 m0, s50
	s_nop 0
	global_load_lds_dwordx4 v[224:225], off
	s_waitcnt vmcnt(8)
	s_waitcnt lgkmcnt(0)
	s_barrier
	s_cbranch_vccnz .LBB0_1005
	s_setprio 1
	s_waitcnt lgkmcnt(0)
	v_mfma_f32_16x16x32_bf16 v[66:69], v[150:153], v[190:193], v[66:69]
	v_mfma_f32_16x16x32_bf16 v[62:65], v[158:161], v[190:193], v[62:65]
	v_mfma_f32_16x16x32_bf16 v[50:53], v[150:153], v[178:181], v[50:53]
	v_mfma_f32_16x16x32_bf16 v[46:49], v[158:161], v[178:181], v[46:49]
	v_mfma_f32_16x16x32_bf16 v[34:37], v[150:153], v[174:177], v[34:37]
	v_mfma_f32_16x16x32_bf16 v[30:33], v[158:161], v[174:177], v[30:33]
	v_mfma_f32_16x16x32_bf16 v[18:21], v[150:153], v[166:169], v[18:21]
	v_mfma_f32_16x16x32_bf16 v[14:17], v[158:161], v[166:169], v[14:17]
	v_mfma_f32_16x16x32_bf16 v[66:69], v[154:157], v[194:197], v[66:69]
	v_mfma_f32_16x16x32_bf16 v[62:65], v[162:165], v[194:197], v[62:65]
	v_mfma_f32_16x16x32_bf16 v[50:53], v[154:157], v[182:185], v[50:53]
	v_mfma_f32_16x16x32_bf16 v[46:49], v[162:165], v[182:185], v[46:49]
	v_mfma_f32_16x16x32_bf16 v[34:37], v[154:157], v[186:189], v[34:37]
	v_mfma_f32_16x16x32_bf16 v[30:33], v[162:165], v[186:189], v[30:33]
	v_mfma_f32_16x16x32_bf16 v[18:21], v[154:157], v[170:173], v[18:21]
	v_mfma_f32_16x16x32_bf16 v[14:17], v[162:165], v[170:173], v[14:17]
	s_setprio 0
	s_setprio 1
	v_mfma_f32_16x16x32_bf16 v[58:61], v[134:137], v[190:193], v[58:61]
	v_mfma_f32_16x16x32_bf16 v[54:57], v[142:145], v[190:193], v[54:57]
	v_mfma_f32_16x16x32_bf16 v[42:45], v[134:137], v[178:181], v[42:45]
	v_mfma_f32_16x16x32_bf16 v[38:41], v[142:145], v[178:181], v[38:41]
	v_mfma_f32_16x16x32_bf16 v[26:29], v[134:137], v[174:177], v[26:29]
	v_mfma_f32_16x16x32_bf16 v[22:25], v[142:145], v[174:177], v[22:25]
	v_mfma_f32_16x16x32_bf16 v[10:13], v[134:137], v[166:169], v[10:13]
	v_mfma_f32_16x16x32_bf16 v[6:9], v[142:145], v[166:169], v[6:9]
	v_mfma_f32_16x16x32_bf16 v[58:61], v[138:141], v[194:197], v[58:61]
	v_mfma_f32_16x16x32_bf16 v[54:57], v[146:149], v[194:197], v[54:57]
	v_mfma_f32_16x16x32_bf16 v[42:45], v[138:141], v[182:185], v[42:45]
	v_mfma_f32_16x16x32_bf16 v[38:41], v[146:149], v[182:185], v[38:41]
	v_mfma_f32_16x16x32_bf16 v[26:29], v[138:141], v[186:189], v[26:29]
	v_mfma_f32_16x16x32_bf16 v[22:25], v[146:149], v[186:189], v[22:25]
	v_mfma_f32_16x16x32_bf16 v[10:13], v[138:141], v[170:173], v[10:13]
	v_mfma_f32_16x16x32_bf16 v[6:9], v[146:149], v[170:173], v[6:9]
	s_setprio 0
	s_branch .LBB0_1005

; #define PG8_STAGE(bufoff, gbase, voff) do { _Pragma("unroll") for (int _i = 0; _i < 2; ++_i) \
;         __builtin_amdgcn_global_load_lds((const unsigned*)((const char*)(gbase) + (voff)[_i]), (LAS unsigned*)(lds + (bufoff) + ldsw + _i * 8192), 16, 0, 0); } while (0)
; #define PG8_LDA(dst, b, h) do { _Pragma("unroll") for (int m = 0; m < 4; ++m) _Pragma("unroll") for (int k = 0; k < 2; ++k) dst[m][k] = *(const LAS bf16x8*)(lds + PG8_SA(b, h) + ((aoff ^ (k * 64)) + m * 2048)); } while (0)
; #define PG8_LDB(dst, b, h) do { _Pragma("unroll") for (int n = 0; n < 2; ++n) _Pragma("unroll") for (int k = 0; k < 2; ++k) dst[n][k] = *(const LAS bf16x8*)(lds + PG8_SB(b, h) + ((boff ^ (k * 64)) + n * 2048)); } while (0)
; #define PG8_BAR __builtin_amdgcn_s_barrier()
;     ...
;             const bool last = (t == nt - 2);
;             const char* a1 = cA + (size_t)(t + 1) * kstepA;
;             const char* a2 = last ? nA : cA + (size_t)(t + 2) * kstepA; const char* b2 = last ? nB : cB + (size_t)(t + 2) * kstepB;
;             const char* a3 = a2 + kstepA; const char* b3 = b2 + kstepB;
;             unsigned vs[2][2];
;             if constexpr (GATHER) {
;                 if (last && has_next) {
; #pragma unroll
;                     for (int hh = 0; hh < 2; ++hh)
; #pragma unroll
;                         for (int i = 0; i < 2; ++i) voffN[hh][i] = (unsigned)idxl[(ui + 1) * 256 + hh * HALF + sR[i]] * (unsigned)(K * 2) + (unsigned)sC[i] * 2u;
;                 }
; #pragma unroll
;                 for (int hh = 0; hh < 2; ++hh)
; #pragma unroll
;                     for (int i = 0; i < 2; ++i) vs[hh][i] = last ? voffN[hh][i] : voffA[hh][i];
;             } else {
; #pragma unroll
;                 for (int hh = 0; hh < 2; ++hh)
; #pragma unroll
;                     for (int i = 0; i < 2; ++i) vs[hh][i] = voffA[hh][i];
;             }
;             PG8_LDB(B0, 0, 0); PG8_LDB(B1, 0, 1); PG8_SCHED; PG8_LDA(At, 0, 0); PG8_STAGE(PG8_SA(1, 1), a1, voffA[1]);
;             PG8_WAIT_V(8); PG8_WAIT_L(0); PG8_BAR; if (do0) { PG8_MMA(0, 0, At, B0); PG8_MMA(0, 1, At, B1); } PG8_BAR; PG8_SCHED;
;             PG8_LDA(At, 0, 1); PG8_STAGE(PG8_SB(0, 0), b2, voffB); PG8_STAGE(PG8_SB(0, 1), b2 + hstep, voffB); PG8_STAGE(PG8_SA(0, 0), a2, vs[0]);
;             PG8_WAIT_V(8); PG8_WAIT_L(0); PG8_BAR; if (do1) { PG8_MMA(1, 0, At, B0); PG8_MMA(1, 1, At, B1); } PG8_BAR; PG8_SCHED;
.LBB0_1102:
	s_add_u32 s8, s22, 0x4000
	s_addc_u32 s9, s23, 0
	s_cmp_eq_u32 s61, s59
	s_cselect_b32 s27, s15, s9
	s_cselect_b32 s26, s14, s8
	s_cselect_b32 s25, s17, s63
	s_cselect_b32 s24, s16, s62
	s_barrier
	s_mov_b32 m0, s29
	v_lshl_add_u64 v[4:5], s[24:25], 0, v[208:209]
	s_add_u32 s8, s24, 0xb0000
	s_waitcnt lgkmcnt(0)
	ds_read_b128 v[190:193], v226 offset:16384
	ds_read_b128 v[178:181], v226 offset:18432
	ds_read_b128 v[194:197], v227 offset:16384
	ds_read_b128 v[182:185], v227 offset:18432
	ds_read_b128 v[174:177], v226 offset:20480
	ds_read_b128 v[166:169], v226 offset:22528
	ds_read_b128 v[186:189], v227 offset:20480
	ds_read_b128 v[170:173], v227 offset:22528
	global_load_lds_dwordx4 v[4:5], off nt
	v_lshl_add_u64 v[4:5], s[24:25], 0, v[210:211]
	s_mov_b32 m0, s30
	s_addc_u32 s9, s25, 0
	global_load_lds_dwordx4 v[4:5], off nt
	v_lshl_add_u64 v[4:5], s[8:9], 0, v[208:209]
	s_mov_b32 m0, s31
	v_cndmask_b32_e64 v3, 0, 1, s[18:19]
	global_load_lds_dwordx4 v[4:5], off nt
	v_lshl_add_u64 v[4:5], s[8:9], 0, v[210:211]
	s_mov_b32 m0, s34
	v_cmp_ne_u32_e64 s[8:9], 1, v3
	global_load_lds_dwordx4 v[4:5], off nt
	v_lshl_add_u64 v[4:5], s[26:27], 0, v[200:201]
	s_mov_b32 m0, s28
	s_andn2_b64 vcc, exec, s[18:19]
	global_load_lds_dwordx4 v[4:5], off
	v_lshl_add_u64 v[4:5], s[26:27], 0, v[202:203]
	s_mov_b32 m0, s35
	s_nop 0
	global_load_lds_dwordx4 v[4:5], off
	s_waitcnt vmcnt(8)
	s_waitcnt lgkmcnt(0)
	s_barrier
	s_cbranch_vccnz .LBB0_1104
	s_setprio 1
	s_waitcnt lgkmcnt(0)
	v_mfma_f32_16x16x32_bf16 v[130:133], v[150:153], v[190:193], v[130:133]
	v_mfma_f32_16x16x32_bf16 v[126:129], v[158:161], v[190:193], v[126:129]
	v_mfma_f32_16x16x32_bf16 v[114:117], v[150:153], v[178:181], v[114:117]
	v_mfma_f32_16x16x32_bf16 v[110:113], v[158:161], v[178:181], v[110:113]
	v_mfma_f32_16x16x32_bf16 v[98:101], v[150:153], v[174:177], v[98:101]
	v_mfma_f32_16x16x32_bf16 v[94:97], v[158:161], v[174:177], v[94:97]
	v_mfma_f32_16x16x32_bf16 v[82:85], v[150:153], v[166:169], v[82:85]
	v_mfma_f32_16x16x32_bf16 v[78:81], v[158:161], v[166:169], v[78:81]
	v_mfma_f32_16x16x32_bf16 v[130:133], v[154:157], v[194:197], v[130:133]
	v_mfma_f32_16x16x32_bf16 v[126:129], v[162:165], v[194:197], v[126:129]
	v_mfma_f32_16x16x32_bf16 v[114:117], v[154:157], v[182:185], v[114:117]
	v_mfma_f32_16x16x32_bf16 v[110:113], v[162:165], v[182:185], v[110:113]
	v_mfma_f32_16x16x32_bf16 v[98:101], v[154:157], v[186:189], v[98:101]
	v_mfma_f32_16x16x32_bf16 v[94:97], v[162:165], v[186:189], v[94:97]
	v_mfma_f32_16x16x32_bf16 v[82:85], v[154:157], v[170:173], v[82:85]
	v_mfma_f32_16x16x32_bf16 v[78:81], v[162:165], v[170:173], v[78:81]
	s_setprio 0
	s_setprio 1
	v_mfma_f32_16x16x32_bf16 v[122:125], v[134:137], v[190:193], v[122:125]
	v_mfma_f32_16x16x32_bf16 v[118:121], v[142:145], v[190:193], v[118:121]
	v_mfma_f32_16x16x32_bf16 v[106:109], v[134:137], v[178:181], v[106:109]
	v_mfma_f32_16x16x32_bf16 v[102:105], v[142:145], v[178:181], v[102:105]
	v_mfma_f32_16x16x32_bf16 v[90:93], v[134:137], v[174:177], v[90:93]
	v_mfma_f32_16x16x32_bf16 v[86:89], v[142:145], v[174:177], v[86:89]
	v_mfma_f32_16x16x32_bf16 v[74:77], v[134:137], v[166:169], v[74:77]
	v_mfma_f32_16x16x32_bf16 v[70:73], v[142:145], v[166:169], v[70:73]
	v_mfma_f32_16x16x32_bf16 v[122:125], v[138:141], v[194:197], v[122:125]
	v_mfma_f32_16x16x32_bf16 v[118:121], v[146:149], v[194:197], v[118:121]
	v_mfma_f32_16x16x32_bf16 v[106:109], v[138:141], v[182:185], v[106:109]
	v_mfma_f32_16x16x32_bf16 v[102:105], v[146:149], v[182:185], v[102:105]
	v_mfma_f32_16x16x32_bf16 v[90:93], v[138:141], v[186:189], v[90:93]
	v_mfma_f32_16x16x32_bf16 v[86:89], v[146:149], v[186:189], v[86:89]
	v_mfma_f32_16x16x32_bf16 v[74:77], v[138:141], v[170:173], v[74:77]
	v_mfma_f32_16x16x32_bf16 v[70:73], v[146:149], v[170:173], v[70:73]
	s_setprio 0

; #define PG8_STAGE(bufoff, gbase, voff) do { _Pragma("unroll") for (int _i = 0; _i < 2; ++_i) \
;         __builtin_amdgcn_global_load_lds((const unsigned*)((const char*)(gbase) + (voff)[_i]), (LAS unsigned*)(lds + (bufoff) + ldsw + _i * 8192), 16, 0, 0); } while (0)
; #define PG8_LDA(dst, b, h) do { _Pragma("unroll") for (int m = 0; m < 4; ++m) _Pragma("unroll") for (int k = 0; k < 2; ++k) dst[m][k] = *(const LAS bf16x8*)(lds + PG8_SA(b, h) + ((aoff ^ (k * 64)) + m * 2048)); } while (0)
;     ...
;             const char* a3 = a2 + kstepA; const char* b3 = b2 + kstepB;
;             unsigned vs[2][2];
;             if constexpr (GATHER) {
;                 if (last && has_next) {
; #pragma unroll
;                     for (int hh = 0; hh < 2; ++hh)
; #pragma unroll
;                         for (int i = 0; i < 2; ++i) voffN[hh][i] = (unsigned)idxl[(ui + 1) * 256 + hh * HALF + sR[i]] * (unsigned)(K * 2) + (unsigned)sC[i] * 2u;
;                 }
; #pragma unroll
;                 for (int hh = 0; hh < 2; ++hh)
; #pragma unroll
;                     for (int i = 0; i < 2; ++i) vs[hh][i] = last ? voffN[hh][i] : voffA[hh][i];
;             } else {
; #pragma unroll
;                 for (int hh = 0; hh < 2; ++hh)
; #pragma unroll
;                     for (int i = 0; i < 2; ++i) vs[hh][i] = voffA[hh][i];
;             }
;             PG8_LDB(B0, 0, 0); PG8_LDB(B1, 0, 1); PG8_SCHED; PG8_LDA(At, 0, 0); PG8_STAGE(PG8_SA(1, 1), a1, voffA[1]);
;             PG8_WAIT_V(8); PG8_WAIT_L(0); PG8_BAR; if (do0) { PG8_MMA(0, 0, At, B0); PG8_MMA(0, 1, At, B1); } PG8_BAR; PG8_SCHED;
;             PG8_LDA(At, 0, 1); PG8_STAGE(PG8_SB(0, 0), b2, voffB); PG8_STAGE(PG8_SB(0, 1), b2 + hstep, voffB); PG8_STAGE(PG8_SA(0, 0), a2, vs[0]);
;             PG8_WAIT_V(8); PG8_WAIT_L(0); PG8_BAR; if (do1) { PG8_MMA(1, 0, At, B0); PG8_MMA(1, 1, At, B1); } PG8_BAR; PG8_SCHED;
;             PG8_LDB(B0, 1, 0); PG8_LDB(B1, 1, 1); PG8_SCHED; PG8_LDA(At, 1, 0); PG8_STAGE(PG8_SA(0, 1), a2, vs[1]);
;             PG8_WAIT_V(8); PG8_WAIT_L(0); PG8_BAR; if (do0) { PG8_MMA(0, 0, At, B0); PG8_MMA(0, 1, At, B1); } PG8_BAR; PG8_SCHED;
;             PG8_LDA(At, 1, 1); PG8_STAGE(PG8_SB(1, 0), b3, voffB); PG8_STAGE(PG8_SB(1, 1), b3 + hstep, voffB); PG8_STAGE(PG8_SA(1, 0), a3, vs[0]);
;             PG8_WAIT_V(8); PG8_WAIT_L(0); PG8_BAR; if (do1) { PG8_MMA(1, 0, At, B0); PG8_MMA(1, 1, At, B1); } PG8_BAR; PG8_SCHED;
.LBB0_1106:
	s_add_u32 s6, s26, 0x4000
	s_addc_u32 s7, s27, 0
	s_add_u32 s26, s24, 0x4000
	s_addc_u32 s27, s25, 0
	s_barrier
	s_mov_b32 m0, s39
	v_lshl_add_u64 v[4:5], s[26:27], 0, v[208:209]
	s_add_u32 s24, s24, 0xb4000
	s_waitcnt lgkmcnt(0)
	ds_read_b128 v[190:193], v226 offset:49152
	ds_read_b128 v[178:181], v226 offset:51200
	ds_read_b128 v[194:197], v227 offset:49152
	ds_read_b128 v[182:185], v227 offset:51200
	ds_read_b128 v[174:177], v226 offset:53248
	ds_read_b128 v[166:169], v226 offset:55296
	ds_read_b128 v[186:189], v227 offset:53248
	ds_read_b128 v[170:173], v227 offset:55296
	global_load_lds_dwordx4 v[4:5], off nt
	v_lshl_add_u64 v[4:5], s[26:27], 0, v[210:211]
	s_mov_b32 m0, s40
	s_addc_u32 s25, s25, 0
	global_load_lds_dwordx4 v[4:5], off nt
	v_lshl_add_u64 v[4:5], s[24:25], 0, v[208:209]
	s_mov_b32 m0, s43
	s_and_b64 vcc, exec, s[8:9]
	global_load_lds_dwordx4 v[4:5], off nt
	v_lshl_add_u64 v[4:5], s[24:25], 0, v[210:211]
	s_mov_b32 m0, s44
	s_nop 0
	global_load_lds_dwordx4 v[4:5], off nt
	v_lshl_add_u64 v[4:5], s[6:7], 0, v[200:201]
	s_mov_b32 m0, s41
	s_nop 0
	global_load_lds_dwordx4 v[4:5], off
	v_lshl_add_u64 v[4:5], s[6:7], 0, v[202:203]
	s_mov_b32 m0, s42
	s_nop 0
	global_load_lds_dwordx4 v[4:5], off
	s_waitcnt vmcnt(8)
	s_waitcnt lgkmcnt(0)
	s_barrier
	s_cbranch_vccnz .LBB0_1099
	s_setprio 1
	s_waitcnt lgkmcnt(0)
	v_mfma_f32_16x16x32_bf16 v[130:133], v[150:153], v[190:193], v[130:133]
	v_mfma_f32_16x16x32_bf16 v[126:129], v[158:161], v[190:193], v[126:129]
	v_mfma_f32_16x16x32_bf16 v[114:117], v[150:153], v[178:181], v[114:117]
	v_mfma_f32_16x16x32_bf16 v[110:113], v[158:161], v[178:181], v[110:113]
	v_mfma_f32_16x16x32_bf16 v[98:101], v[150:153], v[174:177], v[98:101]
	v_mfma_f32_16x16x32_bf16 v[94:97], v[158:161], v[174:177], v[94:97]
	v_mfma_f32_16x16x32_bf16 v[82:85], v[150:153], v[166:169], v[82:85]
	v_mfma_f32_16x16x32_bf16 v[78:81], v[158:161], v[166:169], v[78:81]
	v_mfma_f32_16x16x32_bf16 v[130:133], v[154:157], v[194:197], v[130:133]
	v_mfma_f32_16x16x32_bf16 v[126:129], v[162:165], v[194:197], v[126:129]
	v_mfma_f32_16x16x32_bf16 v[114:117], v[154:157], v[182:185], v[114:117]
	v_mfma_f32_16x16x32_bf16 v[110:113], v[162:165], v[182:185], v[110:113]
	v_mfma_f32_16x16x32_bf16 v[98:101], v[154:157], v[186:189], v[98:101]
	v_mfma_f32_16x16x32_bf16 v[94:97], v[162:165], v[186:189], v[94:97]
	v_mfma_f32_16x16x32_bf16 v[82:85], v[154:157], v[170:173], v[82:85]
	v_mfma_f32_16x16x32_bf16 v[78:81], v[162:165], v[170:173], v[78:81]
	s_setprio 0
	s_setprio 1
	v_mfma_f32_16x16x32_bf16 v[122:125], v[134:137], v[190:193], v[122:125]
	v_mfma_f32_16x16x32_bf16 v[118:121], v[142:145], v[190:193], v[118:121]
	v_mfma_f32_16x16x32_bf16 v[106:109], v[134:137], v[178:181], v[106:109]
	v_mfma_f32_16x16x32_bf16 v[102:105], v[142:145], v[178:181], v[102:105]
	v_mfma_f32_16x16x32_bf16 v[90:93], v[134:137], v[174:177], v[90:93]
	v_mfma_f32_16x16x32_bf16 v[86:89], v[142:145], v[174:177], v[86:89]
	v_mfma_f32_16x16x32_bf16 v[74:77], v[134:137], v[166:169], v[74:77]
	v_mfma_f32_16x16x32_bf16 v[70:73], v[142:145], v[166:169], v[70:73]
	v_mfma_f32_16x16x32_bf16 v[122:125], v[138:141], v[194:197], v[122:125]
	v_mfma_f32_16x16x32_bf16 v[118:121], v[146:149], v[194:197], v[118:121]
	v_mfma_f32_16x16x32_bf16 v[106:109], v[138:141], v[182:185], v[106:109]
	v_mfma_f32_16x16x32_bf16 v[102:105], v[146:149], v[182:185], v[102:105]
	v_mfma_f32_16x16x32_bf16 v[90:93], v[138:141], v[186:189], v[90:93]
	v_mfma_f32_16x16x32_bf16 v[86:89], v[146:149], v[186:189], v[86:89]
	v_mfma_f32_16x16x32_bf16 v[74:77], v[138:141], v[170:173], v[74:77]
	v_mfma_f32_16x16x32_bf16 v[70:73], v[146:149], v[170:173], v[70:73]
	s_setprio 0
	s_branch .LBB0_1099

; #define PG8_STAGE(bufoff, gbase, voff) do { _Pragma("unroll") for (int _i = 0; _i < 2; ++_i) \
;         __builtin_amdgcn_global_load_lds((const unsigned*)((const char*)(gbase) + (voff)[_i]), (LAS unsigned*)(lds + (bufoff) + ldsw + _i * 8192), 16, 0, 0); } while (0)
; #define PG8_LDA(dst, b, h) do { _Pragma("unroll") for (int m = 0; m < 4; ++m) _Pragma("unroll") for (int k = 0; k < 2; ++k) dst[m][k] = *(const LAS bf16x8*)(lds + PG8_SA(b, h) + ((aoff ^ (k * 64)) + m * 2048)); } while (0)
; #define PG8_LDB(dst, b, h) do { _Pragma("unroll") for (int n = 0; n < 2; ++n) _Pragma("unroll") for (int k = 0; k < 2; ++k) dst[n][k] = *(const LAS bf16x8*)(lds + PG8_SB(b, h) + ((boff ^ (k * 64)) + n * 2048)); } while (0)
; #define PG8_WAIT_V(n) asm volatile("s_waitcnt vmcnt(" #n ")" ::: "memory")
; #define PG8_WAIT_L(n) asm volatile("s_waitcnt lgkmcnt(" #n ")" ::: "memory")
;     ...
;             const char* a2 = last ? nA : cA + (size_t)(t + 2) * kstepA; const char* b2 = last ? nB : cB + (size_t)(t + 2) * kstepB;
;             const char* a3 = a2 + kstepA; const char* b3 = b2 + kstepB;
;             unsigned vs[2][2];
;             if constexpr (GATHER) {
;                 if (last && has_next) {
; #pragma unroll
;                     for (int hh = 0; hh < 2; ++hh)
; #pragma unroll
;                         for (int i = 0; i < 2; ++i) voffN[hh][i] = (unsigned)idxl[(ui + 1) * 256 + hh * HALF + sR[i]] * (unsigned)(K * 2) + (unsigned)sC[i] * 2u;
;                 }
; #pragma unroll
;                 for (int hh = 0; hh < 2; ++hh)
; #pragma unroll
;                     for (int i = 0; i < 2; ++i) vs[hh][i] = last ? voffN[hh][i] : voffA[hh][i];
;             } else {
; #pragma unroll
;                 for (int hh = 0; hh < 2; ++hh)
; #pragma unroll
;                     for (int i = 0; i < 2; ++i) vs[hh][i] = voffA[hh][i];
;             }
;             PG8_LDB(B0, 0, 0); PG8_LDB(B1, 0, 1); PG8_SCHED; PG8_LDA(At, 0, 0); PG8_STAGE(PG8_SA(1, 1), a1, voffA[1]);
;             PG8_WAIT_V(8); PG8_WAIT_L(0); PG8_BAR; if (do0) { PG8_MMA(0, 0, At, B0); PG8_MMA(0, 1, At, B1); } PG8_BAR; PG8_SCHED;
;             PG8_LDA(At, 0, 1); PG8_STAGE(PG8_SB(0, 0), b2, voffB); PG8_STAGE(PG8_SB(0, 1), b2 + hstep, voffB); PG8_STAGE(PG8_SA(0, 0), a2, vs[0]);
;             PG8_WAIT_V(8); PG8_WAIT_L(0); PG8_BAR; if (do1) { PG8_MMA(1, 0, At, B0); PG8_MMA(1, 1, At, B1); } PG8_BAR; PG8_SCHED;
.LBB0_2337:
	v_add_u32_e32 v136, s43, v159
	v_add_u32_e32 v145, s43, v160
	ds_read_b128 v[166:169], v136
	ds_read_b128 v[170:173], v145
	v_add_u32_e32 v136, s44, v159
	s_add_u32 s22, s90, s20
	v_add_u32_e32 v145, s44, v160
	ds_read_b128 v[174:177], v136
	ds_read_b128 v[178:181], v145
	v_add_u32_e32 v136, s45, v159
	s_addc_u32 s23, s91, s21
	v_add_u32_e32 v145, s45, v160
	ds_read_b128 v[182:185], v136
	ds_read_b128 v[186:189], v145
	v_add_u32_e32 v136, s46, v159
	s_add_u32 s24, s22, 0x4213700
	v_add_u32_e32 v145, s46, v160
	ds_read_b128 v[190:193], v136
	ds_read_b128 v[194:197], v145
	s_addc_u32 s25, s23, 0
	s_and_b64 s[22:23], s[2:3], exec
	s_cselect_b32 s22, s14, s13
	s_cselect_b32 s27, s83, s25
	s_cselect_b32 s26, s82, s24
	s_cselect_b32 s23, s15, s53
	s_add_u32 s24, s22, 0x4000
	s_addc_u32 s25, s23, 0
	v_cndmask_b32_e64 v136, v152, v146, s[2:3]
	v_cndmask_b32_e64 v232, v153, v147, s[2:3]
	v_cndmask_b32_e64 v145, v148, v164, s[2:3]
	v_cndmask_b32_e64 v149, v150, v165, s[2:3]
	v_lshl_add_u64 v[234:235], v[156:157], 0, s[20:21]
	s_add_i32 m0, s17, 0xc000
	ds_read_b128 v[200:203], v161
	ds_read_b128 v[204:207], v161 offset:2048
	ds_read_b128 v[208:211], v162
	ds_read_b128 v[212:215], v162 offset:2048
	ds_read_b128 v[216:219], v161 offset:4096
	ds_read_b128 v[220:223], v161 offset:6144
	ds_read_b128 v[224:227], v162 offset:4096
	ds_read_b128 v[228:231], v162 offset:6144
	global_load_lds_dwordx4 v[234:235], off
	v_lshl_add_u64 v[234:235], v[154:155], 0, s[20:21]
	s_add_i32 m0, s17, 0xe000
	s_nop 0
	global_load_lds_dwordx4 v[234:235], off
	s_waitcnt vmcnt(8)
	s_waitcnt lgkmcnt(0)
	s_barrier
	s_setprio 1
	s_waitcnt lgkmcnt(0)
	v_mfma_f32_16x16x32_bf16 v[126:129], v[166:169], v[200:203], v[126:129]
	v_mfma_f32_16x16x32_bf16 v[122:125], v[174:177], v[200:203], v[122:125]
	v_mfma_f32_16x16x32_bf16 v[110:113], v[166:169], v[204:207], v[110:113]
	v_mfma_f32_16x16x32_bf16 v[106:109], v[174:177], v[204:207], v[106:109]
	v_mfma_f32_16x16x32_bf16 v[94:97], v[166:169], v[216:219], v[94:97]
	v_mfma_f32_16x16x32_bf16 v[90:93], v[174:177], v[216:219], v[90:93]
	v_mfma_f32_16x16x32_bf16 v[78:81], v[166:169], v[220:223], v[78:81]
	v_mfma_f32_16x16x32_bf16 v[74:77], v[174:177], v[220:223], v[74:77]
	v_mfma_f32_16x16x32_bf16 v[126:129], v[170:173], v[208:211], v[126:129]
	v_mfma_f32_16x16x32_bf16 v[122:125], v[178:181], v[208:211], v[122:125]
	v_mfma_f32_16x16x32_bf16 v[110:113], v[170:173], v[212:215], v[110:113]
	v_mfma_f32_16x16x32_bf16 v[106:109], v[178:181], v[212:215], v[106:109]
	v_mfma_f32_16x16x32_bf16 v[94:97], v[170:173], v[224:227], v[94:97]
	v_mfma_f32_16x16x32_bf16 v[90:93], v[178:181], v[224:227], v[90:93]
	v_mfma_f32_16x16x32_bf16 v[78:81], v[170:173], v[228:231], v[78:81]
	v_mfma_f32_16x16x32_bf16 v[74:77], v[178:181], v[228:231], v[74:77]
	s_setprio 0
	s_setprio 1
	v_mfma_f32_16x16x32_bf16 v[118:121], v[182:185], v[200:203], v[118:121]
	v_mfma_f32_16x16x32_bf16 v[114:117], v[190:193], v[200:203], v[114:117]
	v_mfma_f32_16x16x32_bf16 v[102:105], v[182:185], v[204:207], v[102:105]
	v_mfma_f32_16x16x32_bf16 v[98:101], v[190:193], v[204:207], v[98:101]
	v_mfma_f32_16x16x32_bf16 v[86:89], v[182:185], v[216:219], v[86:89]
	v_mfma_f32_16x16x32_bf16 v[82:85], v[190:193], v[216:219], v[82:85]
	v_mfma_f32_16x16x32_bf16 v[70:73], v[182:185], v[220:223], v[70:73]
	v_mfma_f32_16x16x32_bf16 v[66:69], v[190:193], v[220:223], v[66:69]
	v_mfma_f32_16x16x32_bf16 v[118:121], v[186:189], v[208:211], v[118:121]
	v_mfma_f32_16x16x32_bf16 v[114:117], v[194:197], v[208:211], v[114:117]
	v_mfma_f32_16x16x32_bf16 v[102:105], v[186:189], v[212:215], v[102:105]
	v_mfma_f32_16x16x32_bf16 v[98:101], v[194:197], v[212:215], v[98:101]
	v_mfma_f32_16x16x32_bf16 v[86:89], v[186:189], v[224:227], v[86:89]
	v_mfma_f32_16x16x32_bf16 v[82:85], v[194:197], v[224:227], v[82:85]
	v_mfma_f32_16x16x32_bf16 v[70:73], v[186:189], v[228:231], v[70:73]
	v_mfma_f32_16x16x32_bf16 v[66:69], v[194:197], v[228:231], v[66:69]
	s_setprio 0
	s_barrier
	s_add_i32 s2, s43, s34
	v_lshl_add_u64 v[234:235], s[22:23], 0, v[132:133]
	s_mov_b32 m0, s2
	ds_read_b128 v[200:203], v161 offset:16384
	ds_read_b128 v[204:207], v161 offset:18432
	ds_read_b128 v[208:211], v162 offset:16384
	ds_read_b128 v[212:215], v162 offset:18432
	ds_read_b128 v[216:219], v161 offset:20480
	ds_read_b128 v[220:223], v161 offset:22528
	ds_read_b128 v[224:227], v162 offset:20480
	ds_read_b128 v[228:231], v162 offset:22528
	global_load_lds_dwordx4 v[234:235], off nt
	s_add_i32 m0, s2, 0x2000
	s_add_u32 s2, s22, 0x40000
	v_lshl_add_u64 v[234:235], s[22:23], 0, v[134:135]
	s_addc_u32 s3, s23, 0
	s_add_i32 s55, s45, s34
	global_load_lds_dwordx4 v[234:235], off nt
	v_lshl_add_u64 v[234:235], s[2:3], 0, v[132:133]
	s_mov_b32 m0, s55
	v_mov_b32_e32 v233, v137
	global_load_lds_dwordx4 v[234:235], off nt
	v_lshl_add_u64 v[234:235], s[2:3], 0, v[134:135]
	s_add_i32 m0, s55, 0x2000
	s_nop 0
	global_load_lds_dwordx4 v[234:235], off nt
	s_mov_b32 m0, s17
	v_lshl_add_u64 v[234:235], s[26:27], 0, v[136:137]
	global_load_lds_dwordx4 v136, s[26:27]
	s_mov_b32 m0, s35
	s_nop 0
	global_load_lds_dwordx4 v232, s[26:27]
	s_waitcnt vmcnt(8)
	s_waitcnt lgkmcnt(0)
	v_lshl_add_u64 v[232:233], s[26:27], 0, v[232:233]
	s_barrier
; #define PG8_STAGE(bufoff, gbase, voff) do { _Pragma("unroll") for (int _i = 0; _i < 2; ++_i) \
;         __builtin_amdgcn_global_load_lds((const unsigned*)((const char*)(gbase) + (voff)[_i]), (LAS unsigned*)(lds + (bufoff) + ldsw + _i * 8192), 16, 0, 0); } while (0)
; #define PG8_LDA(dst, b, h) do { _Pragma("unroll") for (int m = 0; m < 4; ++m) _Pragma("unroll") for (int k = 0; k < 2; ++k) dst[m][k] = *(const LAS bf16x8*)(lds + PG8_SA(b, h) + ((aoff ^ (k * 64)) + m * 2048)); } while (0)
; #define PG8_LDB(dst, b, h) do { _Pragma("unroll") for (int n = 0; n < 2; ++n) _Pragma("unroll") for (int k = 0; k < 2; ++k) dst[n][k] = *(const LAS bf16x8*)(lds + PG8_SB(b, h) + ((boff ^ (k * 64)) + n * 2048)); } while (0)
; #define PG8_MMA(ai, bj, At, Bt) do { __builtin_amdgcn_s_setprio(1); _Pragma("unroll") for (int m = 0; m < 4; ++m) _Pragma("unroll") for (int n = 0; n < 2; ++n) _Pragma("unroll") for (int k = 0; k < 2; ++k) \
;         acc[ai][bj][m][n] = __builtin_amdgcn_mfma_f32_16x16x32_bf16(Bt[n][k], At[m][k], acc[ai][bj][m][n], 0, 0, 0); __builtin_amdgcn_s_setprio(0); } while (0)
; #define PG8_WAIT_V(n) asm volatile("s_waitcnt vmcnt(" #n ")" ::: "memory")
; #define PG8_WAIT_L(n) asm volatile("s_waitcnt lgkmcnt(" #n ")" ::: "memory")
; #define PG8_BAR __builtin_amdgcn_s_barrier()
; #define PG8_SCHED __builtin_amdgcn_sched_barrier(0)
;     ...
;             PG8_WAIT_V(8); PG8_WAIT_L(0); PG8_BAR; if (do1) { PG8_MMA(1, 0, At, B0); PG8_MMA(1, 1, At, B1); } PG8_BAR; PG8_SCHED;
;             PG8_LDB(B0, 1, 0); PG8_LDB(B1, 1, 1); PG8_SCHED; PG8_LDA(At, 1, 0); PG8_STAGE(PG8_SA(0, 1), a2, vs[1]);
;             PG8_WAIT_V(8); PG8_WAIT_L(0); PG8_BAR; if (do0) { PG8_MMA(0, 0, At, B0); PG8_MMA(0, 1, At, B1); } PG8_BAR; PG8_SCHED;
	s_setprio 1
	s_waitcnt lgkmcnt(0)
	v_mfma_f32_16x16x32_bf16 v[62:65], v[166:169], v[200:203], v[62:65]
	v_mfma_f32_16x16x32_bf16 v[58:61], v[174:177], v[200:203], v[58:61]
	v_mfma_f32_16x16x32_bf16 v[46:49], v[166:169], v[204:207], v[46:49]
	v_mfma_f32_16x16x32_bf16 v[42:45], v[174:177], v[204:207], v[42:45]
	v_mfma_f32_16x16x32_bf16 v[30:33], v[166:169], v[216:219], v[30:33]
	v_mfma_f32_16x16x32_bf16 v[26:29], v[174:177], v[216:219], v[26:29]
	v_mfma_f32_16x16x32_bf16 v[14:17], v[166:169], v[220:223], v[14:17]
	v_mfma_f32_16x16x32_bf16 v[10:13], v[174:177], v[220:223], v[10:13]
	v_mfma_f32_16x16x32_bf16 v[62:65], v[170:173], v[208:211], v[62:65]
	v_mfma_f32_16x16x32_bf16 v[58:61], v[178:181], v[208:211], v[58:61]
	v_mfma_f32_16x16x32_bf16 v[46:49], v[170:173], v[212:215], v[46:49]
	v_mfma_f32_16x16x32_bf16 v[42:45], v[178:181], v[212:215], v[42:45]
	v_mfma_f32_16x16x32_bf16 v[30:33], v[170:173], v[224:227], v[30:33]
	v_mfma_f32_16x16x32_bf16 v[26:29], v[178:181], v[224:227], v[26:29]
	v_mfma_f32_16x16x32_bf16 v[14:17], v[170:173], v[228:231], v[14:17]
	v_mfma_f32_16x16x32_bf16 v[10:13], v[178:181], v[228:231], v[10:13]
	s_setprio 0
	s_setprio 1
	v_mfma_f32_16x16x32_bf16 v[54:57], v[182:185], v[200:203], v[54:57]
	v_mfma_f32_16x16x32_bf16 v[50:53], v[190:193], v[200:203], v[50:53]
	v_mfma_f32_16x16x32_bf16 v[38:41], v[182:185], v[204:207], v[38:41]
	v_mfma_f32_16x16x32_bf16 v[34:37], v[190:193], v[204:207], v[34:37]
	v_mfma_f32_16x16x32_bf16 v[22:25], v[182:185], v[216:219], v[22:25]
	v_mfma_f32_16x16x32_bf16 v[18:21], v[190:193], v[216:219], v[18:21]
	v_mfma_f32_16x16x32_bf16 v[6:9], v[182:185], v[220:223], v[6:9]
	v_mfma_f32_16x16x32_bf16 v[2:5], v[190:193], v[220:223], v[2:5]
	v_mfma_f32_16x16x32_bf16 v[54:57], v[186:189], v[208:211], v[54:57]
	v_mfma_f32_16x16x32_bf16 v[50:53], v[194:197], v[208:211], v[50:53]
	v_mfma_f32_16x16x32_bf16 v[38:41], v[186:189], v[212:215], v[38:41]
	v_mfma_f32_16x16x32_bf16 v[34:37], v[194:197], v[212:215], v[34:37]
	v_mfma_f32_16x16x32_bf16 v[22:25], v[186:189], v[224:227], v[22:25]
	v_mfma_f32_16x16x32_bf16 v[18:21], v[194:197], v[224:227], v[18:21]
	v_mfma_f32_16x16x32_bf16 v[6:9], v[186:189], v[228:231], v[6:9]
	v_mfma_f32_16x16x32_bf16 v[2:5], v[194:197], v[228:231], v[2:5]
	s_setprio 0
	s_barrier
	s_add_i32 s2, 0, 0x18000
	v_add_u32_e32 v136, s2, v159
	v_add_u32_e32 v151, s2, v160
	ds_read_b128 v[166:169], v136
	ds_read_b128 v[170:173], v151
	v_add_u32_e32 v136, s47, v159
	s_add_i32 s55, 0, 0x1c000
	v_add_u32_e32 v151, s47, v160
	ds_read_b128 v[174:177], v136
	ds_read_b128 v[178:181], v151
	v_add_u32_e32 v136, s55, v159
	v_add_u32_e32 v151, s55, v160
	ds_read_b128 v[182:185], v136
	ds_read_b128 v[186:189], v151
	v_add_u32_e32 v136, s48, v159
	v_add_u32_e32 v151, s48, v160
	ds_read_b128 v[190:193], v136
	ds_read_b128 v[194:197], v151
	s_mov_b32 m0, s36
	ds_read_b128 v[200:203], v161 offset:32768
	ds_read_b128 v[204:207], v161 offset:34816
	ds_read_b128 v[208:211], v162 offset:32768
	ds_read_b128 v[212:215], v162 offset:34816
	ds_read_b128 v[216:219], v161 offset:36864
	ds_read_b128 v[220:223], v161 offset:38912
	ds_read_b128 v[224:227], v162 offset:36864
	ds_read_b128 v[228:231], v162 offset:38912
	global_load_lds_dwordx4 v145, s[26:27]
	s_mov_b32 m0, s37
	s_nop 0
	global_load_lds_dwordx4 v149, s[26:27]
	s_waitcnt vmcnt(8)
	s_waitcnt lgkmcnt(0)
	s_barrier
	s_setprio 1
	s_waitcnt lgkmcnt(0)
	v_mfma_f32_16x16x32_bf16 v[126:129], v[166:169], v[200:203], v[126:129]
	v_mfma_f32_16x16x32_bf16 v[122:125], v[174:177], v[200:203], v[122:125]
	v_mfma_f32_16x16x32_bf16 v[110:113], v[166:169], v[204:207], v[110:113]
	v_mfma_f32_16x16x32_bf16 v[106:109], v[174:177], v[204:207], v[106:109]
	v_mfma_f32_16x16x32_bf16 v[94:97], v[166:169], v[216:219], v[94:97]
	v_mfma_f32_16x16x32_bf16 v[90:93], v[174:177], v[216:219], v[90:93]
	v_mfma_f32_16x16x32_bf16 v[78:81], v[166:169], v[220:223], v[78:81]
	v_mfma_f32_16x16x32_bf16 v[74:77], v[174:177], v[220:223], v[74:77]
	v_mfma_f32_16x16x32_bf16 v[126:129], v[170:173], v[208:211], v[126:129]
	v_mfma_f32_16x16x32_bf16 v[122:125], v[178:181], v[208:211], v[122:125]
	v_mfma_f32_16x16x32_bf16 v[110:113], v[170:173], v[212:215], v[110:113]
	v_mfma_f32_16x16x32_bf16 v[106:109], v[178:181], v[212:215], v[106:109]
	v_mfma_f32_16x16x32_bf16 v[94:97], v[170:173], v[224:227], v[94:97]
	v_mfma_f32_16x16x32_bf16 v[90:93], v[178:181], v[224:227], v[90:93]
	v_mfma_f32_16x16x32_bf16 v[78:81], v[170:173], v[228:231], v[78:81]
	v_mfma_f32_16x16x32_bf16 v[74:77], v[178:181], v[228:231], v[74:77]
	s_setprio 0
	s_setprio 1
	v_mfma_f32_16x16x32_bf16 v[118:121], v[182:185], v[200:203], v[118:121]
	v_mfma_f32_16x16x32_bf16 v[114:117], v[190:193], v[200:203], v[114:117]
	v_mfma_f32_16x16x32_bf16 v[102:105], v[182:185], v[204:207], v[102:105]
	v_mfma_f32_16x16x32_bf16 v[98:101], v[190:193], v[204:207], v[98:101]
	v_mfma_f32_16x16x32_bf16 v[86:89], v[182:185], v[216:219], v[86:89]
	v_mfma_f32_16x16x32_bf16 v[82:85], v[190:193], v[216:219], v[82:85]
	v_mfma_f32_16x16x32_bf16 v[70:73], v[182:185], v[220:223], v[70:73]
	v_mfma_f32_16x16x32_bf16 v[66:69], v[190:193], v[220:223], v[66:69]
	v_mfma_f32_16x16x32_bf16 v[118:121], v[186:189], v[208:211], v[118:121]
	v_mfma_f32_16x16x32_bf16 v[114:117], v[194:197], v[208:211], v[114:117]
	v_mfma_f32_16x16x32_bf16 v[102:105], v[186:189], v[212:215], v[102:105]
	v_mfma_f32_16x16x32_bf16 v[98:101], v[194:197], v[212:215], v[98:101]
	v_mfma_f32_16x16x32_bf16 v[86:89], v[186:189], v[224:227], v[86:89]
	v_mfma_f32_16x16x32_bf16 v[82:85], v[194:197], v[224:227], v[82:85]
	v_mfma_f32_16x16x32_bf16 v[70:73], v[186:189], v[228:231], v[70:73]
	v_mfma_f32_16x16x32_bf16 v[66:69], v[194:197], v[228:231], v[66:69]
	s_setprio 0
	s_barrier
; #define PG8_STAGE(bufoff, gbase, voff) do { _Pragma("unroll") for (int _i = 0; _i < 2; ++_i) \
;         __builtin_amdgcn_global_load_lds((const unsigned*)((const char*)(gbase) + (voff)[_i]), (LAS unsigned*)(lds + (bufoff) + ldsw + _i * 8192), 16, 0, 0); } while (0)
; #define PG8_LDA(dst, b, h) do { _Pragma("unroll") for (int m = 0; m < 4; ++m) _Pragma("unroll") for (int k = 0; k < 2; ++k) dst[m][k] = *(const LAS bf16x8*)(lds + PG8_SA(b, h) + ((aoff ^ (k * 64)) + m * 2048)); } while (0)
; #define PG8_MMA(ai, bj, At, Bt) do { __builtin_amdgcn_s_setprio(1); _Pragma("unroll") for (int m = 0; m < 4; ++m) _Pragma("unroll") for (int n = 0; n < 2; ++n) _Pragma("unroll") for (int k = 0; k < 2; ++k) \
;         acc[ai][bj][m][n] = __builtin_amdgcn_mfma_f32_16x16x32_bf16(Bt[n][k], At[m][k], acc[ai][bj][m][n], 0, 0, 0); __builtin_amdgcn_s_setprio(0); } while (0)
; #define PG8_WAIT_V(n) asm volatile("s_waitcnt vmcnt(" #n ")" ::: "memory")
; #define PG8_WAIT_L(n) asm volatile("s_waitcnt lgkmcnt(" #n ")" ::: "memory")
; #define PG8_BAR __builtin_amdgcn_s_barrier()
; #define PG8_SCHED __builtin_amdgcn_sched_barrier(0)
;     ...
;             PG8_LDA(At, 1, 1); PG8_STAGE(PG8_SB(1, 0), b3, voffB); PG8_STAGE(PG8_SB(1, 1), b3 + hstep, voffB); PG8_STAGE(PG8_SA(1, 0), a3, vs[0]);
;             PG8_WAIT_V(8); PG8_WAIT_L(0); PG8_BAR; if (do1) { PG8_MMA(1, 0, At, B0); PG8_MMA(1, 1, At, B1); } PG8_BAR; PG8_SCHED;
;         }
	s_add_i32 s2, s2, s34
	v_lshl_add_u64 v[236:237], s[24:25], 0, v[132:133]
	s_mov_b32 m0, s2
	ds_read_b128 v[200:203], v161 offset:49152
	ds_read_b128 v[204:207], v161 offset:51200
	ds_read_b128 v[208:211], v162 offset:49152
	ds_read_b128 v[212:215], v162 offset:51200
	ds_read_b128 v[216:219], v161 offset:53248
	ds_read_b128 v[220:223], v161 offset:55296
	ds_read_b128 v[224:227], v162 offset:53248
	ds_read_b128 v[228:231], v162 offset:55296
	global_load_lds_dwordx4 v[236:237], off nt
	s_add_i32 m0, s2, 0x2000
	s_add_u32 s2, s22, 0x44000
	v_lshl_add_u64 v[236:237], s[24:25], 0, v[134:135]
	s_addc_u32 s3, s23, 0
	s_add_i32 s22, s55, s34
	global_load_lds_dwordx4 v[236:237], off nt
	v_lshl_add_u64 v[236:237], s[2:3], 0, v[132:133]
	s_mov_b32 m0, s22
	v_lshl_add_u64 v[234:235], v[234:235], 0, s[10:11]
	global_load_lds_dwordx4 v[236:237], off nt
	v_lshl_add_u64 v[236:237], s[2:3], 0, v[134:135]
	s_add_i32 m0, s22, 0x2000
	v_lshl_add_u64 v[232:233], v[232:233], 0, s[10:11]
	global_load_lds_dwordx4 v[236:237], off nt
	s_mov_b32 m0, s41
	s_nop 0
	global_load_lds_dwordx4 v[234:235], off
	s_mov_b32 m0, s42
	s_nop 0
	global_load_lds_dwordx4 v[232:233], off
	s_waitcnt vmcnt(8)
	s_waitcnt lgkmcnt(0)
	s_barrier
	s_setprio 1
	s_waitcnt lgkmcnt(0)
	v_mfma_f32_16x16x32_bf16 v[62:65], v[166:169], v[200:203], v[62:65]
	v_mfma_f32_16x16x32_bf16 v[58:61], v[174:177], v[200:203], v[58:61]
	v_mfma_f32_16x16x32_bf16 v[46:49], v[166:169], v[204:207], v[46:49]
	v_mfma_f32_16x16x32_bf16 v[42:45], v[174:177], v[204:207], v[42:45]
	v_mfma_f32_16x16x32_bf16 v[30:33], v[166:169], v[216:219], v[30:33]
	v_mfma_f32_16x16x32_bf16 v[26:29], v[174:177], v[216:219], v[26:29]
	v_mfma_f32_16x16x32_bf16 v[14:17], v[166:169], v[220:223], v[14:17]
	v_mfma_f32_16x16x32_bf16 v[10:13], v[174:177], v[220:223], v[10:13]
	v_mfma_f32_16x16x32_bf16 v[62:65], v[170:173], v[208:211], v[62:65]
	v_mfma_f32_16x16x32_bf16 v[58:61], v[178:181], v[208:211], v[58:61]
	v_mfma_f32_16x16x32_bf16 v[46:49], v[170:173], v[212:215], v[46:49]
	v_mfma_f32_16x16x32_bf16 v[42:45], v[178:181], v[212:215], v[42:45]
	v_mfma_f32_16x16x32_bf16 v[30:33], v[170:173], v[224:227], v[30:33]
	v_mfma_f32_16x16x32_bf16 v[26:29], v[178:181], v[224:227], v[26:29]
	v_mfma_f32_16x16x32_bf16 v[14:17], v[170:173], v[228:231], v[14:17]
	v_mfma_f32_16x16x32_bf16 v[10:13], v[178:181], v[228:231], v[10:13]
	s_setprio 0
	s_setprio 1
	v_mfma_f32_16x16x32_bf16 v[54:57], v[182:185], v[200:203], v[54:57]
	v_mfma_f32_16x16x32_bf16 v[50:53], v[190:193], v[200:203], v[50:53]
	v_mfma_f32_16x16x32_bf16 v[38:41], v[182:185], v[204:207], v[38:41]
	v_mfma_f32_16x16x32_bf16 v[34:37], v[190:193], v[204:207], v[34:37]
	v_mfma_f32_16x16x32_bf16 v[22:25], v[182:185], v[216:219], v[22:25]
	v_mfma_f32_16x16x32_bf16 v[18:21], v[190:193], v[216:219], v[18:21]
	v_mfma_f32_16x16x32_bf16 v[6:9], v[182:185], v[220:223], v[6:9]
	v_mfma_f32_16x16x32_bf16 v[2:5], v[190:193], v[220:223], v[2:5]
	v_mfma_f32_16x16x32_bf16 v[54:57], v[186:189], v[208:211], v[54:57]
	v_mfma_f32_16x16x32_bf16 v[50:53], v[194:197], v[208:211], v[50:53]
	v_mfma_f32_16x16x32_bf16 v[38:41], v[186:189], v[212:215], v[38:41]
	v_mfma_f32_16x16x32_bf16 v[34:37], v[194:197], v[212:215], v[34:37]
	v_mfma_f32_16x16x32_bf16 v[22:25], v[186:189], v[224:227], v[22:25]
	v_mfma_f32_16x16x32_bf16 v[18:21], v[194:197], v[224:227], v[18:21]
	v_mfma_f32_16x16x32_bf16 v[6:9], v[186:189], v[228:231], v[6:9]
	v_mfma_f32_16x16x32_bf16 v[2:5], v[194:197], v[228:231], v[2:5]
	s_setprio 0
	s_barrier
	s_add_i32 s54, s54, 2
	s_add_u32 s13, s13, 0x8000
	s_addc_u32 s53, s53, 0
	s_add_u32 s20, s20, 0x100
	s_addc_u32 s21, s21, 0
	s_cmp_gt_u32 s54, 13
	s_cbranch_scc1 .LBB0_2340

; #define PG8_STAGE(bufoff, gbase, voff) do { _Pragma("unroll") for (int _i = 0; _i < 2; ++_i) \
;         __builtin_amdgcn_global_load_lds((const unsigned*)((const char*)(gbase) + (voff)[_i]), (LAS unsigned*)(lds + (bufoff) + ldsw + _i * 8192), 16, 0, 0); } while (0)
; #define PG8_LDA(dst, b, h) do { _Pragma("unroll") for (int m = 0; m < 4; ++m) _Pragma("unroll") for (int k = 0; k < 2; ++k) dst[m][k] = *(const LAS bf16x8*)(lds + PG8_SA(b, h) + ((aoff ^ (k * 64)) + m * 2048)); } while (0)
; #define PG8_LDB(dst, b, h) do { _Pragma("unroll") for (int n = 0; n < 2; ++n) _Pragma("unroll") for (int k = 0; k < 2; ++k) dst[n][k] = *(const LAS bf16x8*)(lds + PG8_SB(b, h) + ((boff ^ (k * 64)) + n * 2048)); } while (0)
; #define PG8_MMA(ai, bj, At, Bt) do { __builtin_amdgcn_s_setprio(1); _Pragma("unroll") for (int m = 0; m < 4; ++m) _Pragma("unroll") for (int n = 0; n < 2; ++n) _Pragma("unroll") for (int k = 0; k < 2; ++k) \
;         acc[ai][bj][m][n] = __builtin_amdgcn_mfma_f32_16x16x32_bf16(Bt[n][k], At[m][k], acc[ai][bj][m][n], 0, 0, 0); __builtin_amdgcn_s_setprio(0); } while (0)
; #define PG8_WAIT_V(n) asm volatile("s_waitcnt vmcnt(" #n ")" ::: "memory")
; #define PG8_WAIT_L(n) asm volatile("s_waitcnt lgkmcnt(" #n ")" ::: "memory")
; #define PG8_BAR __builtin_amdgcn_s_barrier()
; #define PG8_SCHED __builtin_amdgcn_sched_barrier(0)
;     ...
;             PG8_LDB(B0, 0, 0); PG8_LDB(B1, 0, 1); PG8_SCHED; PG8_LDA(At, 0, 0); PG8_STAGE(PG8_SA(1, 1), a1, voffA[1]);
;             PG8_WAIT_V(8); PG8_WAIT_L(0); PG8_BAR; if (do0) { PG8_MMA(0, 0, At, B0); PG8_MMA(0, 1, At, B1); } PG8_BAR; PG8_SCHED;
;             PG8_LDA(At, 0, 1); PG8_STAGE(PG8_SB(0, 0), b2, voffB); PG8_STAGE(PG8_SB(0, 1), b2 + hstep, voffB); PG8_STAGE(PG8_SA(0, 0), a2, vs[0]);
;             PG8_WAIT_V(8); PG8_WAIT_L(0); PG8_BAR; if (do1) { PG8_MMA(1, 0, At, B0); PG8_MMA(1, 1, At, B1); } PG8_BAR; PG8_SCHED;
.LBB0_2411:
	ds_read_b128 v[146:149], v153
	ds_read_b128 v[168:171], v154
	ds_read_b128 v[172:175], v155
	ds_read_b128 v[176:179], v156
	ds_read_b128 v[180:183], v157
	ds_read_b128 v[184:187], v158
	ds_read_b128 v[188:191], v159
	ds_read_b128 v[192:195], v160
	s_add_u32 s20, s18, 0x4000
	s_addc_u32 s21, s19, 0
	s_cmp_eq_u32 s56, 40
	s_cselect_b32 s26, s14, s20
	s_cselect_b32 s27, s15, s21
	s_cselect_b32 s22, s16, s54
	s_cselect_b32 s23, s17, s55
	s_add_u32 s20, s26, 0x4000
	s_addc_u32 s21, s27, 0
	v_lshl_add_u64 v[196:197], s[18:19], 0, v[142:143]
	s_add_i32 m0, s34, 0xc000
	ds_read_b128 v[200:203], v161
	ds_read_b128 v[204:207], v161 offset:2048
	ds_read_b128 v[208:211], v162
	ds_read_b128 v[212:215], v162 offset:2048
	ds_read_b128 v[216:219], v161 offset:4096
	ds_read_b128 v[220:223], v161 offset:6144
	ds_read_b128 v[224:227], v162 offset:4096
	ds_read_b128 v[228:231], v162 offset:6144
	global_load_lds_dwordx4 v[196:197], off
	v_lshl_add_u64 v[196:197], s[18:19], 0, v[144:145]
	s_add_i32 m0, s34, 0xe000
	s_add_u32 s24, s22, 0x4000
	global_load_lds_dwordx4 v[196:197], off
	s_waitcnt vmcnt(8)
	s_waitcnt lgkmcnt(0)
	s_addc_u32 s25, s23, 0
	s_barrier
	s_setprio 1
	s_waitcnt lgkmcnt(0)
	v_mfma_f32_16x16x32_bf16 v[126:129], v[146:149], v[200:203], v[126:129]
	v_mfma_f32_16x16x32_bf16 v[122:125], v[172:175], v[200:203], v[122:125]
	v_mfma_f32_16x16x32_bf16 v[114:117], v[146:149], v[204:207], v[114:117]
	v_mfma_f32_16x16x32_bf16 v[106:109], v[172:175], v[204:207], v[106:109]
	v_mfma_f32_16x16x32_bf16 v[98:101], v[146:149], v[216:219], v[98:101]
	v_mfma_f32_16x16x32_bf16 v[90:93], v[172:175], v[216:219], v[90:93]
	v_mfma_f32_16x16x32_bf16 v[82:85], v[146:149], v[220:223], v[82:85]
	v_mfma_f32_16x16x32_bf16 v[74:77], v[172:175], v[220:223], v[74:77]
	v_mfma_f32_16x16x32_bf16 v[126:129], v[168:171], v[208:211], v[126:129]
	v_mfma_f32_16x16x32_bf16 v[122:125], v[176:179], v[208:211], v[122:125]
	v_mfma_f32_16x16x32_bf16 v[114:117], v[168:171], v[212:215], v[114:117]
	v_mfma_f32_16x16x32_bf16 v[106:109], v[176:179], v[212:215], v[106:109]
	v_mfma_f32_16x16x32_bf16 v[98:101], v[168:171], v[224:227], v[98:101]
	v_mfma_f32_16x16x32_bf16 v[90:93], v[176:179], v[224:227], v[90:93]
	v_mfma_f32_16x16x32_bf16 v[82:85], v[168:171], v[228:231], v[82:85]
	v_mfma_f32_16x16x32_bf16 v[74:77], v[176:179], v[228:231], v[74:77]
	s_setprio 0
	s_setprio 1
	v_mfma_f32_16x16x32_bf16 v[118:121], v[180:183], v[200:203], v[118:121]
	v_mfma_f32_16x16x32_bf16 v[110:113], v[188:191], v[200:203], v[110:113]
	v_mfma_f32_16x16x32_bf16 v[102:105], v[180:183], v[204:207], v[102:105]
	v_mfma_f32_16x16x32_bf16 v[94:97], v[188:191], v[204:207], v[94:97]
	v_mfma_f32_16x16x32_bf16 v[86:89], v[180:183], v[216:219], v[86:89]
	v_mfma_f32_16x16x32_bf16 v[78:81], v[188:191], v[216:219], v[78:81]
	v_mfma_f32_16x16x32_bf16 v[70:73], v[180:183], v[220:223], v[70:73]
	v_mfma_f32_16x16x32_bf16 v[66:69], v[188:191], v[220:223], v[66:69]
	v_mfma_f32_16x16x32_bf16 v[118:121], v[184:187], v[208:211], v[118:121]
	v_mfma_f32_16x16x32_bf16 v[110:113], v[192:195], v[208:211], v[110:113]
	v_mfma_f32_16x16x32_bf16 v[102:105], v[184:187], v[212:215], v[102:105]
	v_mfma_f32_16x16x32_bf16 v[94:97], v[192:195], v[212:215], v[94:97]
	v_mfma_f32_16x16x32_bf16 v[86:89], v[184:187], v[224:227], v[86:89]
	v_mfma_f32_16x16x32_bf16 v[78:81], v[192:195], v[224:227], v[78:81]
	v_mfma_f32_16x16x32_bf16 v[70:73], v[184:187], v[228:231], v[70:73]
	v_mfma_f32_16x16x32_bf16 v[66:69], v[192:195], v[228:231], v[66:69]
	s_setprio 0
	s_barrier
	s_add_i32 s57, s42, s30
	v_lshl_add_u64 v[196:197], s[22:23], 0, v[132:133]
	s_mov_b32 m0, s57
	ds_read_b128 v[200:203], v161 offset:16384
	ds_read_b128 v[204:207], v161 offset:18432
	ds_read_b128 v[208:211], v162 offset:16384
	ds_read_b128 v[212:215], v162 offset:18432
	ds_read_b128 v[216:219], v161 offset:20480
	ds_read_b128 v[220:223], v161 offset:22528
	ds_read_b128 v[224:227], v162 offset:20480
	ds_read_b128 v[228:231], v162 offset:22528
	global_load_lds_dwordx4 v[196:197], off nt
	s_add_i32 m0, s57, 0x2000
	s_add_u32 s58, s22, 0xb0000
	v_lshl_add_u64 v[196:197], s[22:23], 0, v[130:131]
	s_addc_u32 s59, s23, 0
	s_add_i32 s57, s43, s30
	global_load_lds_dwordx4 v[196:197], off nt
	v_lshl_add_u64 v[196:197], s[58:59], 0, v[132:133]
	s_mov_b32 m0, s57
	s_nop 0
	global_load_lds_dwordx4 v[196:197], off nt
	v_lshl_add_u64 v[196:197], s[58:59], 0, v[130:131]
	s_add_i32 m0, s57, 0x2000
	s_nop 0
	global_load_lds_dwordx4 v[196:197], off nt
	v_lshl_add_u64 v[196:197], s[26:27], 0, v[134:135]
	s_mov_b32 m0, s34
	s_nop 0
	global_load_lds_dwordx4 v[196:197], off
	v_lshl_add_u64 v[196:197], s[26:27], 0, v[136:137]
	s_mov_b32 m0, s35
	s_nop 0
	global_load_lds_dwordx4 v[196:197], off
	s_waitcnt vmcnt(8)
	s_waitcnt lgkmcnt(0)
	s_barrier
; #define PG8_STAGE(bufoff, gbase, voff) do { _Pragma("unroll") for (int _i = 0; _i < 2; ++_i) \
;         __builtin_amdgcn_global_load_lds((const unsigned*)((const char*)(gbase) + (voff)[_i]), (LAS unsigned*)(lds + (bufoff) + ldsw + _i * 8192), 16, 0, 0); } while (0)
; #define PG8_LDA(dst, b, h) do { _Pragma("unroll") for (int m = 0; m < 4; ++m) _Pragma("unroll") for (int k = 0; k < 2; ++k) dst[m][k] = *(const LAS bf16x8*)(lds + PG8_SA(b, h) + ((aoff ^ (k * 64)) + m * 2048)); } while (0)
; #define PG8_LDB(dst, b, h) do { _Pragma("unroll") for (int n = 0; n < 2; ++n) _Pragma("unroll") for (int k = 0; k < 2; ++k) dst[n][k] = *(const LAS bf16x8*)(lds + PG8_SB(b, h) + ((boff ^ (k * 64)) + n * 2048)); } while (0)
; #define PG8_MMA(ai, bj, At, Bt) do { __builtin_amdgcn_s_setprio(1); _Pragma("unroll") for (int m = 0; m < 4; ++m) _Pragma("unroll") for (int n = 0; n < 2; ++n) _Pragma("unroll") for (int k = 0; k < 2; ++k) \
;         acc[ai][bj][m][n] = __builtin_amdgcn_mfma_f32_16x16x32_bf16(Bt[n][k], At[m][k], acc[ai][bj][m][n], 0, 0, 0); __builtin_amdgcn_s_setprio(0); } while (0)
; #define PG8_WAIT_V(n) asm volatile("s_waitcnt vmcnt(" #n ")" ::: "memory")
; #define PG8_WAIT_L(n) asm volatile("s_waitcnt lgkmcnt(" #n ")" ::: "memory")
; #define PG8_BAR __builtin_amdgcn_s_barrier()
; #define PG8_SCHED __builtin_amdgcn_sched_barrier(0)
;     ...
;             PG8_WAIT_V(8); PG8_WAIT_L(0); PG8_BAR; if (do1) { PG8_MMA(1, 0, At, B0); PG8_MMA(1, 1, At, B1); } PG8_BAR; PG8_SCHED;
;             PG8_LDB(B0, 1, 0); PG8_LDB(B1, 1, 1); PG8_SCHED; PG8_LDA(At, 1, 0); PG8_STAGE(PG8_SA(0, 1), a2, vs[1]);
;             PG8_WAIT_V(8); PG8_WAIT_L(0); PG8_BAR; if (do0) { PG8_MMA(0, 0, At, B0); PG8_MMA(0, 1, At, B1); } PG8_BAR; PG8_SCHED;
	s_setprio 1
	s_waitcnt lgkmcnt(0)
	v_mfma_f32_16x16x32_bf16 v[62:65], v[146:149], v[200:203], v[62:65]
	v_mfma_f32_16x16x32_bf16 v[58:61], v[172:175], v[200:203], v[58:61]
	v_mfma_f32_16x16x32_bf16 v[46:49], v[146:149], v[204:207], v[46:49]
	v_mfma_f32_16x16x32_bf16 v[42:45], v[172:175], v[204:207], v[42:45]
	v_mfma_f32_16x16x32_bf16 v[30:33], v[146:149], v[216:219], v[30:33]
	v_mfma_f32_16x16x32_bf16 v[26:29], v[172:175], v[216:219], v[26:29]
	v_mfma_f32_16x16x32_bf16 v[14:17], v[146:149], v[220:223], v[14:17]
	v_mfma_f32_16x16x32_bf16 v[10:13], v[172:175], v[220:223], v[10:13]
	v_mfma_f32_16x16x32_bf16 v[62:65], v[168:171], v[208:211], v[62:65]
	v_mfma_f32_16x16x32_bf16 v[58:61], v[176:179], v[208:211], v[58:61]
	v_mfma_f32_16x16x32_bf16 v[46:49], v[168:171], v[212:215], v[46:49]
	v_mfma_f32_16x16x32_bf16 v[42:45], v[176:179], v[212:215], v[42:45]
	v_mfma_f32_16x16x32_bf16 v[30:33], v[168:171], v[224:227], v[30:33]
	v_mfma_f32_16x16x32_bf16 v[26:29], v[176:179], v[224:227], v[26:29]
	v_mfma_f32_16x16x32_bf16 v[14:17], v[168:171], v[228:231], v[14:17]
	v_mfma_f32_16x16x32_bf16 v[10:13], v[176:179], v[228:231], v[10:13]
	s_setprio 0
	s_setprio 1
	v_mfma_f32_16x16x32_bf16 v[54:57], v[180:183], v[200:203], v[54:57]
	v_mfma_f32_16x16x32_bf16 v[50:53], v[188:191], v[200:203], v[50:53]
	v_mfma_f32_16x16x32_bf16 v[38:41], v[180:183], v[204:207], v[38:41]
	v_mfma_f32_16x16x32_bf16 v[34:37], v[188:191], v[204:207], v[34:37]
	v_mfma_f32_16x16x32_bf16 v[22:25], v[180:183], v[216:219], v[22:25]
	v_mfma_f32_16x16x32_bf16 v[18:21], v[188:191], v[216:219], v[18:21]
	v_mfma_f32_16x16x32_bf16 v[6:9], v[180:183], v[220:223], v[6:9]
	v_mfma_f32_16x16x32_bf16 v[2:5], v[188:191], v[220:223], v[2:5]
	v_mfma_f32_16x16x32_bf16 v[54:57], v[184:187], v[208:211], v[54:57]
	v_mfma_f32_16x16x32_bf16 v[50:53], v[192:195], v[208:211], v[50:53]
	v_mfma_f32_16x16x32_bf16 v[38:41], v[184:187], v[212:215], v[38:41]
	v_mfma_f32_16x16x32_bf16 v[34:37], v[192:195], v[212:215], v[34:37]
	v_mfma_f32_16x16x32_bf16 v[22:25], v[184:187], v[224:227], v[22:25]
	v_mfma_f32_16x16x32_bf16 v[18:21], v[192:195], v[224:227], v[18:21]
	v_mfma_f32_16x16x32_bf16 v[6:9], v[184:187], v[228:231], v[6:9]
	v_mfma_f32_16x16x32_bf16 v[2:5], v[192:195], v[228:231], v[2:5]
	s_setprio 0
	s_barrier
	s_add_i32 s57, 0, 0x18000
	v_add_u32_e32 v146, s57, v150
	v_add_u32_e32 v167, s57, v151
	s_add_i32 s58, 0, 0x1c000
	ds_read_b128 v[146:149], v146
	ds_read_b128 v[168:171], v167
	ds_read_b128 v[172:175], v163
	ds_read_b128 v[176:179], v164
	v_add_u32_e32 v167, s58, v150
	v_add_u32_e32 v184, s58, v151
	ds_read_b128 v[180:183], v167
	ds_read_b128 v[184:187], v184
	ds_read_b128 v[188:191], v165
	ds_read_b128 v[192:195], v166
	s_mov_b32 m0, s36
	v_lshl_add_u64 v[196:197], s[26:27], 0, v[138:139]
	ds_read_b128 v[200:203], v161 offset:32768
	ds_read_b128 v[204:207], v161 offset:34816
	ds_read_b128 v[208:211], v162 offset:32768
	ds_read_b128 v[212:215], v162 offset:34816
	ds_read_b128 v[216:219], v161 offset:36864
	ds_read_b128 v[220:223], v161 offset:38912
	ds_read_b128 v[224:227], v162 offset:36864
	ds_read_b128 v[228:231], v162 offset:38912
	global_load_lds_dwordx4 v[196:197], off
	v_lshl_add_u64 v[196:197], s[26:27], 0, v[140:141]
	s_mov_b32 m0, s37
	s_nop 0
	global_load_lds_dwordx4 v[196:197], off
	s_waitcnt vmcnt(8)
	s_waitcnt lgkmcnt(0)
	s_barrier
	s_setprio 1
	s_waitcnt lgkmcnt(0)
	v_mfma_f32_16x16x32_bf16 v[126:129], v[146:149], v[200:203], v[126:129]
	v_mfma_f32_16x16x32_bf16 v[122:125], v[172:175], v[200:203], v[122:125]
	v_mfma_f32_16x16x32_bf16 v[114:117], v[146:149], v[204:207], v[114:117]
	v_mfma_f32_16x16x32_bf16 v[106:109], v[172:175], v[204:207], v[106:109]
	v_mfma_f32_16x16x32_bf16 v[98:101], v[146:149], v[216:219], v[98:101]
	v_mfma_f32_16x16x32_bf16 v[90:93], v[172:175], v[216:219], v[90:93]
	v_mfma_f32_16x16x32_bf16 v[82:85], v[146:149], v[220:223], v[82:85]
	v_mfma_f32_16x16x32_bf16 v[74:77], v[172:175], v[220:223], v[74:77]
	v_mfma_f32_16x16x32_bf16 v[126:129], v[168:171], v[208:211], v[126:129]
	v_mfma_f32_16x16x32_bf16 v[122:125], v[176:179], v[208:211], v[122:125]
	v_mfma_f32_16x16x32_bf16 v[114:117], v[168:171], v[212:215], v[114:117]
	v_mfma_f32_16x16x32_bf16 v[106:109], v[176:179], v[212:215], v[106:109]
	v_mfma_f32_16x16x32_bf16 v[98:101], v[168:171], v[224:227], v[98:101]
	v_mfma_f32_16x16x32_bf16 v[90:93], v[176:179], v[224:227], v[90:93]
	v_mfma_f32_16x16x32_bf16 v[82:85], v[168:171], v[228:231], v[82:85]
	v_mfma_f32_16x16x32_bf16 v[74:77], v[176:179], v[228:231], v[74:77]
	s_setprio 0
	s_setprio 1
	v_mfma_f32_16x16x32_bf16 v[118:121], v[180:183], v[200:203], v[118:121]
	v_mfma_f32_16x16x32_bf16 v[110:113], v[188:191], v[200:203], v[110:113]
	v_mfma_f32_16x16x32_bf16 v[102:105], v[180:183], v[204:207], v[102:105]
	v_mfma_f32_16x16x32_bf16 v[94:97], v[188:191], v[204:207], v[94:97]
	v_mfma_f32_16x16x32_bf16 v[86:89], v[180:183], v[216:219], v[86:89]
	v_mfma_f32_16x16x32_bf16 v[78:81], v[188:191], v[216:219], v[78:81]
	v_mfma_f32_16x16x32_bf16 v[70:73], v[180:183], v[220:223], v[70:73]
	v_mfma_f32_16x16x32_bf16 v[66:69], v[188:191], v[220:223], v[66:69]
	v_mfma_f32_16x16x32_bf16 v[118:121], v[184:187], v[208:211], v[118:121]
	v_mfma_f32_16x16x32_bf16 v[110:113], v[192:195], v[208:211], v[110:113]
	v_mfma_f32_16x16x32_bf16 v[102:105], v[184:187], v[212:215], v[102:105]
	v_mfma_f32_16x16x32_bf16 v[94:97], v[192:195], v[212:215], v[94:97]
	v_mfma_f32_16x16x32_bf16 v[86:89], v[184:187], v[224:227], v[86:89]
	v_mfma_f32_16x16x32_bf16 v[78:81], v[192:195], v[224:227], v[78:81]
	v_mfma_f32_16x16x32_bf16 v[70:73], v[184:187], v[228:231], v[70:73]
	v_mfma_f32_16x16x32_bf16 v[66:69], v[192:195], v[228:231], v[66:69]
	s_setprio 0
	s_barrier
; #define PG8_STAGE(bufoff, gbase, voff) do { _Pragma("unroll") for (int _i = 0; _i < 2; ++_i) \
;         __builtin_amdgcn_global_load_lds((const unsigned*)((const char*)(gbase) + (voff)[_i]), (LAS unsigned*)(lds + (bufoff) + ldsw + _i * 8192), 16, 0, 0); } while (0)
; #define PG8_LDA(dst, b, h) do { _Pragma("unroll") for (int m = 0; m < 4; ++m) _Pragma("unroll") for (int k = 0; k < 2; ++k) dst[m][k] = *(const LAS bf16x8*)(lds + PG8_SA(b, h) + ((aoff ^ (k * 64)) + m * 2048)); } while (0)
; #define PG8_MMA(ai, bj, At, Bt) do { __builtin_amdgcn_s_setprio(1); _Pragma("unroll") for (int m = 0; m < 4; ++m) _Pragma("unroll") for (int n = 0; n < 2; ++n) _Pragma("unroll") for (int k = 0; k < 2; ++k) \
;         acc[ai][bj][m][n] = __builtin_amdgcn_mfma_f32_16x16x32_bf16(Bt[n][k], At[m][k], acc[ai][bj][m][n], 0, 0, 0); __builtin_amdgcn_s_setprio(0); } while (0)
; #define PG8_WAIT_V(n) asm volatile("s_waitcnt vmcnt(" #n ")" ::: "memory")
; #define PG8_WAIT_L(n) asm volatile("s_waitcnt lgkmcnt(" #n ")" ::: "memory")
; #define PG8_BAR __builtin_amdgcn_s_barrier()
; #define PG8_SCHED __builtin_amdgcn_sched_barrier(0)
;     ...
;             PG8_LDA(At, 1, 1); PG8_STAGE(PG8_SB(1, 0), b3, voffB); PG8_STAGE(PG8_SB(1, 1), b3 + hstep, voffB); PG8_STAGE(PG8_SA(1, 0), a3, vs[0]);
;             PG8_WAIT_V(8); PG8_WAIT_L(0); PG8_BAR; if (do1) { PG8_MMA(1, 0, At, B0); PG8_MMA(1, 1, At, B1); } PG8_BAR; PG8_SCHED;
;         }
	s_add_i32 s26, s57, s30
	v_lshl_add_u64 v[196:197], s[24:25], 0, v[132:133]
	s_mov_b32 m0, s26
	ds_read_b128 v[200:203], v161 offset:49152
	ds_read_b128 v[204:207], v161 offset:51200
	ds_read_b128 v[208:211], v162 offset:49152
	ds_read_b128 v[212:215], v162 offset:51200
	ds_read_b128 v[216:219], v161 offset:53248
	ds_read_b128 v[220:223], v161 offset:55296
	ds_read_b128 v[224:227], v162 offset:53248
	ds_read_b128 v[228:231], v162 offset:55296
	global_load_lds_dwordx4 v[196:197], off nt
	s_add_i32 m0, s26, 0x2000
	s_add_u32 s22, s22, 0xb4000
	v_lshl_add_u64 v[196:197], s[24:25], 0, v[130:131]
	s_addc_u32 s23, s23, 0
	s_add_i32 s24, s58, s30
	global_load_lds_dwordx4 v[196:197], off nt
	v_lshl_add_u64 v[196:197], s[22:23], 0, v[132:133]
	s_mov_b32 m0, s24
	s_nop 0
	global_load_lds_dwordx4 v[196:197], off nt
	v_lshl_add_u64 v[196:197], s[22:23], 0, v[130:131]
	s_add_i32 m0, s24, 0x2000
	s_nop 0
	global_load_lds_dwordx4 v[196:197], off nt
	v_lshl_add_u64 v[196:197], s[20:21], 0, v[134:135]
	s_mov_b32 m0, s39
	s_nop 0
	global_load_lds_dwordx4 v[196:197], off
	v_lshl_add_u64 v[196:197], s[20:21], 0, v[136:137]
	s_mov_b32 m0, s40
	s_nop 0
	global_load_lds_dwordx4 v[196:197], off
	s_waitcnt vmcnt(8)
	s_waitcnt lgkmcnt(0)
	s_barrier
	s_setprio 1
	s_waitcnt lgkmcnt(0)
	v_mfma_f32_16x16x32_bf16 v[62:65], v[146:149], v[200:203], v[62:65]
	v_mfma_f32_16x16x32_bf16 v[58:61], v[172:175], v[200:203], v[58:61]
	v_mfma_f32_16x16x32_bf16 v[46:49], v[146:149], v[204:207], v[46:49]
	v_mfma_f32_16x16x32_bf16 v[42:45], v[172:175], v[204:207], v[42:45]
	v_mfma_f32_16x16x32_bf16 v[30:33], v[146:149], v[216:219], v[30:33]
	v_mfma_f32_16x16x32_bf16 v[26:29], v[172:175], v[216:219], v[26:29]
	v_mfma_f32_16x16x32_bf16 v[14:17], v[146:149], v[220:223], v[14:17]
	v_mfma_f32_16x16x32_bf16 v[10:13], v[172:175], v[220:223], v[10:13]
	v_mfma_f32_16x16x32_bf16 v[62:65], v[168:171], v[208:211], v[62:65]
	v_mfma_f32_16x16x32_bf16 v[58:61], v[176:179], v[208:211], v[58:61]
	v_mfma_f32_16x16x32_bf16 v[46:49], v[168:171], v[212:215], v[46:49]
	v_mfma_f32_16x16x32_bf16 v[42:45], v[176:179], v[212:215], v[42:45]
	v_mfma_f32_16x16x32_bf16 v[30:33], v[168:171], v[224:227], v[30:33]
	v_mfma_f32_16x16x32_bf16 v[26:29], v[176:179], v[224:227], v[26:29]
	v_mfma_f32_16x16x32_bf16 v[14:17], v[168:171], v[228:231], v[14:17]
	v_mfma_f32_16x16x32_bf16 v[10:13], v[176:179], v[228:231], v[10:13]
	s_setprio 0
	s_setprio 1
	v_mfma_f32_16x16x32_bf16 v[54:57], v[180:183], v[200:203], v[54:57]
	v_mfma_f32_16x16x32_bf16 v[50:53], v[188:191], v[200:203], v[50:53]
	v_mfma_f32_16x16x32_bf16 v[38:41], v[180:183], v[204:207], v[38:41]
	v_mfma_f32_16x16x32_bf16 v[34:37], v[188:191], v[204:207], v[34:37]
	v_mfma_f32_16x16x32_bf16 v[22:25], v[180:183], v[216:219], v[22:25]
	v_mfma_f32_16x16x32_bf16 v[18:21], v[188:191], v[216:219], v[18:21]
	v_mfma_f32_16x16x32_bf16 v[6:9], v[180:183], v[220:223], v[6:9]
	v_mfma_f32_16x16x32_bf16 v[2:5], v[188:191], v[220:223], v[2:5]
	v_mfma_f32_16x16x32_bf16 v[54:57], v[184:187], v[208:211], v[54:57]
	v_mfma_f32_16x16x32_bf16 v[50:53], v[192:195], v[208:211], v[50:53]
	v_mfma_f32_16x16x32_bf16 v[38:41], v[184:187], v[212:215], v[38:41]
	v_mfma_f32_16x16x32_bf16 v[34:37], v[192:195], v[212:215], v[34:37]
	v_mfma_f32_16x16x32_bf16 v[22:25], v[184:187], v[224:227], v[22:25]
	v_mfma_f32_16x16x32_bf16 v[18:21], v[192:195], v[224:227], v[18:21]
	v_mfma_f32_16x16x32_bf16 v[6:9], v[184:187], v[228:231], v[6:9]
	v_mfma_f32_16x16x32_bf16 v[2:5], v[192:195], v[228:231], v[2:5]
	s_setprio 0
	s_barrier
	s_add_i32 s56, s56, 2
	s_add_u32 s18, s18, 0x8000
	s_addc_u32 s19, s19, 0
	s_add_u32 s54, s54, 0x8000
	s_addc_u32 s55, s55, 0
	s_cmp_gt_u32 s56, 41
	s_cbranch_scc0 .LBB0_2411
	s_and_b64 vcc, exec, s[4:5]
	s_cbranch_vccz .LBB0_2414
	s_barrier
